# GEMM K-loops (phases 1,5,6,7,11): back-edge branches straight to the fast trip body, scalar next-tile offset block issued after the LDS fragment reads; stacked on previous changes
# speedup vs baseline: 1.0005x; 1.0005x over previous
.Lp1_join:
	ds_read_b128 v[136:139], v129
	ds_read_b128 v[144:147], v129 offset:2048
	ds_read_b128 v[140:143], v130
	ds_read_b128 v[148:151], v130 offset:2048
	v_add_u32_e32 v129, s86, v246
	v_add_u32_e32 v130, s86, v247
	ds_read_b128 v[152:155], v129
	ds_read_b128 v[160:163], v129 offset:2048
	ds_read_b128 v[156:159], v130
	ds_read_b128 v[164:167], v130 offset:2048
	s_mov_b32 m0, s72
	ds_read_b128 v[168:171], v252
	ds_read_b128 v[176:179], v252 offset:2048
	ds_read_b128 v[172:175], v253
	ds_read_b128 v[180:183], v253 offset:2048
	ds_read_b128 v[184:187], v252 offset:4096
	ds_read_b128 v[192:195], v252 offset:6144
	ds_read_b128 v[188:191], v253 offset:4096
	ds_read_b128 v[196:199], v253 offset:6144
	s_add_i32 s10, s97, 0xffffff80
	s_add_i32 s11, s10, s94
	s_cmpk_eq_i32 s97, 0x880
	s_cselect_b32 s40, s37, s91
	s_cselect_b32 s10, 0, s10
	s_cselect_b32 s39, 0x80, s97
	s_cselect_b32 s38, s36, s11
	s_add_i32 s11, s91, s97
	s_add_i32 s39, s40, s39
	s_addk_i32 s11, 0xff00
	s_add_i32 s40, s40, s10
	buffer_load_dwordx4 v250, s[12:15], s11 offen lds
	s_mov_b32 m0, s75
	s_nop 0
	buffer_load_dwordx4 v251, s[12:15], s11 offen lds
	s_waitcnt vmcnt(8)
	s_waitcnt lgkmcnt(0)
	s_barrier
	s_setprio 1
	s_waitcnt lgkmcnt(5)
	v_mfma_f32_16x16x128_f8f6f4 v[124:127], v[136:143], v[168:175], v[124:127]
	v_mfma_f32_16x16x128_f8f6f4 v[120:123], v[144:151], v[168:175], v[120:123]
	s_waitcnt lgkmcnt(4)
	v_mfma_f32_16x16x128_f8f6f4 v[112:115], v[136:143], v[176:183], v[112:115]
	v_mfma_f32_16x16x128_f8f6f4 v[104:107], v[144:151], v[176:183], v[104:107]
	s_waitcnt lgkmcnt(1)
	v_mfma_f32_16x16x128_f8f6f4 v[96:99], v[136:143], v[184:191], v[96:99]
	v_mfma_f32_16x16x128_f8f6f4 v[128:131], v[144:151], v[184:191], v[88:91]
	s_waitcnt lgkmcnt(0)
	v_mfma_f32_16x16x128_f8f6f4 v[200:203], v[136:143], v[192:199], v[80:83]
	v_mfma_f32_16x16x128_f8f6f4 v[204:207], v[144:151], v[192:199], v[72:75]
	s_setprio 0
	s_setprio 1
	v_mfma_f32_16x16x128_f8f6f4 v[116:119], v[152:159], v[168:175], v[116:119]
	v_mfma_f32_16x16x128_f8f6f4 v[108:111], v[160:167], v[168:175], v[108:111]
	v_mfma_f32_16x16x128_f8f6f4 v[100:103], v[152:159], v[176:183], v[100:103]
	v_mfma_f32_16x16x128_f8f6f4 v[168:171], v[160:167], v[176:183], v[92:95]
	v_mfma_f32_16x16x128_f8f6f4 v[172:175], v[152:159], v[184:191], v[84:87]
	v_mfma_f32_16x16x128_f8f6f4 v[176:179], v[160:167], v[184:191], v[76:79]
	v_mfma_f32_16x16x128_f8f6f4 v[180:183], v[152:159], v[192:199], v[68:71]
	v_mfma_f32_16x16x128_f8f6f4 v[184:187], v[160:167], v[192:199], v[64:67]
	s_setprio 0
	s_barrier
	s_mov_b32 m0, s57
	s_mov_b32 s10, s14
	s_mov_b32 s11, s15
	s_nop 1
	ds_read_b128 v[64:67], v252 offset:16384
	ds_read_b128 v[72:75], v252 offset:18432
	ds_read_b128 v[68:71], v253 offset:16384
	ds_read_b128 v[76:79], v253 offset:18432
	ds_read_b128 v[80:83], v252 offset:20480
	ds_read_b128 v[88:91], v252 offset:22528
	ds_read_b128 v[84:87], v253 offset:20480
	ds_read_b128 v[92:95], v253 offset:22528
	buffer_load_dwordx4 v244, s[8:11], s38 offen lds
	s_mov_b32 m0, s58
	s_add_i32 s41, s38, 0x40000
	buffer_load_dwordx4 v245, s[8:11], s38 offen lds
	s_mov_b32 m0, s59
	s_nop 0
	buffer_load_dwordx4 v244, s[8:11], s41 offen lds
	s_mov_b32 m0, s60
	s_nop 0
	buffer_load_dwordx4 v245, s[8:11], s41 offen lds
	s_mov_b32 m0, s56
	s_nop 0
	buffer_load_dwordx4 v248, s[12:15], s40 offen lds
	s_mov_b32 m0, s61
	s_nop 0
	buffer_load_dwordx4 v249, s[12:15], s40 offen lds
	s_waitcnt vmcnt(8)
	s_waitcnt lgkmcnt(0)
	s_barrier
	s_setprio 1
	s_waitcnt lgkmcnt(5)
	v_mfma_f32_16x16x128_f8f6f4 v[60:63], v[136:143], v[64:71], v[60:63]
	v_mfma_f32_16x16x128_f8f6f4 v[56:59], v[144:151], v[64:71], v[56:59]
	s_waitcnt lgkmcnt(4)
	v_mfma_f32_16x16x128_f8f6f4 v[48:51], v[136:143], v[72:79], v[48:51]
	v_mfma_f32_16x16x128_f8f6f4 v[188:191], v[144:151], v[72:79], v[40:43]
	s_waitcnt lgkmcnt(1)
	v_mfma_f32_16x16x128_f8f6f4 v[192:195], v[136:143], v[80:87], v[32:35]
	v_mfma_f32_16x16x128_f8f6f4 v[196:199], v[144:151], v[80:87], v[24:27]
	s_waitcnt lgkmcnt(0)
	v_mfma_f32_16x16x128_f8f6f4 v[208:211], v[136:143], v[88:95], v[16:19]
	v_mfma_f32_16x16x128_f8f6f4 v[212:215], v[144:151], v[88:95], v[8:11]
	s_setprio 0
	s_setprio 1
	v_mfma_f32_16x16x128_f8f6f4 v[52:55], v[152:159], v[64:71], v[52:55]
	v_mfma_f32_16x16x128_f8f6f4 v[216:219], v[160:167], v[64:71], v[44:47]
	v_mfma_f32_16x16x128_f8f6f4 v[220:223], v[152:159], v[72:79], v[36:39]
	v_mfma_f32_16x16x128_f8f6f4 v[224:227], v[160:167], v[72:79], v[28:31]
	v_mfma_f32_16x16x128_f8f6f4 v[228:231], v[152:159], v[80:87], v[20:23]
	v_mfma_f32_16x16x128_f8f6f4 v[232:235], v[160:167], v[80:87], v[12:15]
	v_mfma_f32_16x16x128_f8f6f4 v[236:239], v[152:159], v[88:95], v[4:7]
	v_mfma_f32_16x16x128_f8f6f4 v[240:243], v[160:167], v[88:95], v[0:3]
	s_setprio 0
	s_barrier
	s_add_i32 s41, 0, 0x18000
	s_nop 2
	v_add_u32_e32 v4, s41, v246
	v_add_u32_e32 v12, s41, v247
	s_add_i32 s41, 0, 0x1c000
	v_add_u32_e32 v16, s41, v246
	ds_read_b128 v[0:3], v4
	ds_read_b128 v[8:11], v4 offset:2048
	ds_read_b128 v[4:7], v12
	ds_read_b128 v[12:15], v12 offset:2048
	v_add_u32_e32 v17, s41, v247
	ds_read_b128 v[136:139], v16
	ds_read_b128 v[144:147], v16 offset:2048
	ds_read_b128 v[140:143], v17
	ds_read_b128 v[148:151], v17 offset:2048
	s_mov_b32 m0, s62
	ds_read_b128 v[16:19], v252 offset:32768
	ds_read_b128 v[24:27], v252 offset:34816
	ds_read_b128 v[20:23], v253 offset:32768
	ds_read_b128 v[28:31], v253 offset:34816
	ds_read_b128 v[32:35], v252 offset:36864
	ds_read_b128 v[40:43], v252 offset:38912
	ds_read_b128 v[36:39], v253 offset:36864
	ds_read_b128 v[44:47], v253 offset:38912
	buffer_load_dwordx4 v250, s[12:15], s40 offen lds
	s_mov_b32 m0, s63
	s_nop 0
	buffer_load_dwordx4 v251, s[12:15], s40 offen lds
	s_waitcnt vmcnt(8)
	s_waitcnt lgkmcnt(0)
	s_barrier
	s_setprio 1
	s_waitcnt lgkmcnt(5)
	v_mfma_f32_16x16x128_f8f6f4 v[124:127], v[0:7], v[16:23], v[124:127]
	v_mfma_f32_16x16x128_f8f6f4 v[120:123], v[8:15], v[16:23], v[120:123]
	s_waitcnt lgkmcnt(4)
	v_mfma_f32_16x16x128_f8f6f4 v[112:115], v[0:7], v[24:31], v[112:115]
	v_mfma_f32_16x16x128_f8f6f4 v[104:107], v[8:15], v[24:31], v[104:107]
	s_waitcnt lgkmcnt(1)
	v_mfma_f32_16x16x128_f8f6f4 v[96:99], v[0:7], v[32:39], v[96:99]
	v_mfma_f32_16x16x128_f8f6f4 v[88:91], v[8:15], v[32:39], v[128:131]
	s_waitcnt lgkmcnt(0)
	v_mfma_f32_16x16x128_f8f6f4 v[80:83], v[0:7], v[40:47], v[200:203]
	v_mfma_f32_16x16x128_f8f6f4 v[72:75], v[8:15], v[40:47], v[204:207]
	s_setprio 0
	s_setprio 1
	v_mfma_f32_16x16x128_f8f6f4 v[116:119], v[136:143], v[16:23], v[116:119]
	v_mfma_f32_16x16x128_f8f6f4 v[108:111], v[144:151], v[16:23], v[108:111]
	v_mfma_f32_16x16x128_f8f6f4 v[100:103], v[136:143], v[24:31], v[100:103]
	v_mfma_f32_16x16x128_f8f6f4 v[92:95], v[144:151], v[24:31], v[168:171]
	v_mfma_f32_16x16x128_f8f6f4 v[84:87], v[136:143], v[32:39], v[172:175]
	v_mfma_f32_16x16x128_f8f6f4 v[76:79], v[144:151], v[32:39], v[176:179]
	v_mfma_f32_16x16x128_f8f6f4 v[68:71], v[136:143], v[40:47], v[180:183]
	v_mfma_f32_16x16x128_f8f6f4 v[64:67], v[144:151], v[40:47], v[184:187]
	s_setprio 0
	s_barrier
	s_mov_b32 m0, s64
	s_add_i32 s40, s38, 0x80
	ds_read_b128 v[152:155], v252 offset:49152
	ds_read_b128 v[160:163], v252 offset:51200
	ds_read_b128 v[156:159], v253 offset:49152
	ds_read_b128 v[164:167], v253 offset:51200
	ds_read_b128 v[168:171], v252 offset:53248
	ds_read_b128 v[176:179], v252 offset:55296
	ds_read_b128 v[172:175], v253 offset:53248
	ds_read_b128 v[180:183], v253 offset:55296
	buffer_load_dwordx4 v244, s[8:11], s40 offen lds
	s_mov_b32 m0, s65
	s_add_i32 s38, s38, 0x40080
	buffer_load_dwordx4 v245, s[8:11], s40 offen lds
	s_mov_b32 m0, s68
	s_nop 0
	buffer_load_dwordx4 v244, s[8:11], s38 offen lds
	s_mov_b32 m0, s69
	s_nop 0
	buffer_load_dwordx4 v245, s[8:11], s38 offen lds
	s_mov_b32 m0, s66
	s_nop 0
	buffer_load_dwordx4 v248, s[12:15], s39 offen lds
	s_mov_b32 m0, s67
	s_nop 0
	buffer_load_dwordx4 v249, s[12:15], s39 offen lds
	s_waitcnt vmcnt(8)
	s_waitcnt lgkmcnt(0)
	s_barrier
	s_setprio 1
	s_waitcnt lgkmcnt(5)
	v_mfma_f32_16x16x128_f8f6f4 v[60:63], v[0:7], v[152:159], v[60:63]
	v_mfma_f32_16x16x128_f8f6f4 v[56:59], v[8:15], v[152:159], v[56:59]
	s_waitcnt lgkmcnt(4)
	v_mfma_f32_16x16x128_f8f6f4 v[48:51], v[0:7], v[160:167], v[48:51]
	v_mfma_f32_16x16x128_f8f6f4 v[40:43], v[8:15], v[160:167], v[188:191]
	s_waitcnt lgkmcnt(1)
	v_mfma_f32_16x16x128_f8f6f4 v[32:35], v[0:7], v[168:175], v[192:195]
	v_mfma_f32_16x16x128_f8f6f4 v[24:27], v[8:15], v[168:175], v[196:199]
	s_waitcnt lgkmcnt(0)
	v_mfma_f32_16x16x128_f8f6f4 v[16:19], v[0:7], v[176:183], v[208:211]
	v_mfma_f32_16x16x128_f8f6f4 v[8:11], v[8:15], v[176:183], v[212:215]
	s_setprio 0
	s_setprio 1
	v_mfma_f32_16x16x128_f8f6f4 v[52:55], v[136:143], v[152:159], v[52:55]
	v_mfma_f32_16x16x128_f8f6f4 v[44:47], v[144:151], v[152:159], v[216:219]
	v_mfma_f32_16x16x128_f8f6f4 v[36:39], v[136:143], v[160:167], v[220:223]
	v_mfma_f32_16x16x128_f8f6f4 v[28:31], v[144:151], v[160:167], v[224:227]
	v_mfma_f32_16x16x128_f8f6f4 v[20:23], v[136:143], v[168:175], v[228:231]
	v_mfma_f32_16x16x128_f8f6f4 v[12:15], v[144:151], v[168:175], v[232:235]
	v_mfma_f32_16x16x128_f8f6f4 v[4:7], v[136:143], v[176:183], v[236:239]
	v_mfma_f32_16x16x128_f8f6f4 v[0:3], v[144:151], v[176:183], v[240:243]
	s_setprio 0
	s_barrier
	s_add_i32 s96, s96, 2
	s_addk_i32 s97, 0x100
	s_cmp_gt_u32 s96, 13
	s_cbranch_scc1 .LBB0_1022
	s_cmpk_lg_i32 s97, 0x780
	s_cbranch_scc1 .Lp1_fast

.Lp5_join:
	ds_read_b128 v[136:139], v129
	ds_read_b128 v[144:147], v129 offset:2048
	ds_read_b128 v[140:143], v130
	ds_read_b128 v[148:151], v130 offset:2048
	v_add_u32_e32 v129, s50, v244
	v_add_u32_e32 v130, s50, v245
	ds_read_b128 v[152:155], v129
	ds_read_b128 v[160:163], v129 offset:2048
	ds_read_b128 v[156:159], v130
	ds_read_b128 v[164:167], v130 offset:2048
	s_mov_b32 m0, s44
	ds_read_b128 v[168:171], v250
	ds_read_b128 v[176:179], v250 offset:2048
	ds_read_b128 v[172:175], v251
	ds_read_b128 v[180:183], v251 offset:2048
	ds_read_b128 v[184:187], v250 offset:4096
	ds_read_b128 v[192:195], v250 offset:6144
	ds_read_b128 v[188:191], v251 offset:4096
	ds_read_b128 v[196:199], v251 offset:6144
	s_add_i32 s6, s62, 0xffffff80
	s_add_i32 s7, s6, s57
	s_cmpk_eq_i32 s62, 0x880
	s_cselect_b32 s65, s35, s54
	s_cselect_b32 s6, 0, s6
	s_cselect_b32 s64, 0x80, s62
	s_cselect_b32 s63, s29, s7
	s_add_i32 s7, s54, s62
	s_add_i32 s64, s65, s64
	s_addk_i32 s7, 0xff00
	s_add_i32 s65, s65, s6
	buffer_load_dwordx4 v248, s[8:11], s7 offen lds
	s_mov_b32 m0, s47
	s_nop 0
	buffer_load_dwordx4 v249, s[8:11], s7 offen lds
	s_waitcnt vmcnt(8)
	s_waitcnt lgkmcnt(0)
	s_barrier
	s_setprio 1
	s_waitcnt lgkmcnt(5)
	v_mfma_f32_16x16x128_f8f6f4 v[124:127], v[136:143], v[168:175], v[124:127]
	v_mfma_f32_16x16x128_f8f6f4 v[120:123], v[144:151], v[168:175], v[120:123]
	s_waitcnt lgkmcnt(4)
	v_mfma_f32_16x16x128_f8f6f4 v[108:111], v[136:143], v[176:183], v[108:111]
	v_mfma_f32_16x16x128_f8f6f4 v[104:107], v[144:151], v[176:183], v[104:107]
	s_waitcnt lgkmcnt(1)
	v_mfma_f32_16x16x128_f8f6f4 v[128:131], v[136:143], v[184:191], v[92:95]
	v_mfma_f32_16x16x128_f8f6f4 v[200:203], v[144:151], v[184:191], v[88:91]
	s_waitcnt lgkmcnt(0)
	v_mfma_f32_16x16x128_f8f6f4 v[204:207], v[136:143], v[192:199], v[76:79]
	v_mfma_f32_16x16x128_f8f6f4 v[208:211], v[144:151], v[192:199], v[72:75]
	s_setprio 0
	s_setprio 1
	v_mfma_f32_16x16x128_f8f6f4 v[116:119], v[152:159], v[168:175], v[116:119]
	v_mfma_f32_16x16x128_f8f6f4 v[112:115], v[160:167], v[168:175], v[112:115]
	v_mfma_f32_16x16x128_f8f6f4 v[100:103], v[152:159], v[176:183], v[100:103]
	v_mfma_f32_16x16x128_f8f6f4 v[96:99], v[160:167], v[176:183], v[96:99]
	v_mfma_f32_16x16x128_f8f6f4 v[168:171], v[152:159], v[184:191], v[84:87]
	v_mfma_f32_16x16x128_f8f6f4 v[172:175], v[160:167], v[184:191], v[80:83]
	v_mfma_f32_16x16x128_f8f6f4 v[176:179], v[152:159], v[192:199], v[68:71]
	v_mfma_f32_16x16x128_f8f6f4 v[180:183], v[160:167], v[192:199], v[64:67]
	s_setprio 0
	s_barrier
	s_mov_b32 m0, s26
	s_mov_b32 s6, s10
	s_mov_b32 s7, s11
	s_nop 1
	ds_read_b128 v[64:67], v250 offset:16384
	ds_read_b128 v[72:75], v250 offset:18432
	ds_read_b128 v[68:71], v251 offset:16384
	ds_read_b128 v[76:79], v251 offset:18432
	ds_read_b128 v[80:83], v250 offset:20480
	ds_read_b128 v[88:91], v250 offset:22528
	ds_read_b128 v[84:87], v251 offset:20480
	ds_read_b128 v[92:95], v251 offset:22528
	buffer_load_dwordx4 v132, s[4:7], s63 offen lds
	s_mov_b32 m0, s27
	s_add_i32 s66, s63, 0x40000
	buffer_load_dwordx4 v133, s[4:7], s63 offen lds
	s_mov_b32 m0, s28
	s_nop 0
	buffer_load_dwordx4 v132, s[4:7], s66 offen lds
	s_mov_b32 m0, s30
	s_nop 0
	buffer_load_dwordx4 v133, s[4:7], s66 offen lds
	s_mov_b32 m0, s25
	s_nop 0
	buffer_load_dwordx4 v246, s[8:11], s65 offen lds
	s_mov_b32 m0, s31
	s_nop 0
	buffer_load_dwordx4 v247, s[8:11], s65 offen lds
	s_waitcnt vmcnt(8)
	s_waitcnt lgkmcnt(0)
	s_barrier
	s_setprio 1
	s_waitcnt lgkmcnt(5)
	v_mfma_f32_16x16x128_f8f6f4 v[60:63], v[136:143], v[64:71], v[60:63]
	v_mfma_f32_16x16x128_f8f6f4 v[56:59], v[144:151], v[64:71], v[56:59]
	s_waitcnt lgkmcnt(4)
	v_mfma_f32_16x16x128_f8f6f4 v[184:187], v[136:143], v[72:79], v[44:47]
	v_mfma_f32_16x16x128_f8f6f4 v[188:191], v[144:151], v[72:79], v[40:43]
	s_waitcnt lgkmcnt(1)
	v_mfma_f32_16x16x128_f8f6f4 v[192:195], v[136:143], v[80:87], v[28:31]
	v_mfma_f32_16x16x128_f8f6f4 v[196:199], v[144:151], v[80:87], v[24:27]
	s_waitcnt lgkmcnt(0)
	v_mfma_f32_16x16x128_f8f6f4 v[212:215], v[136:143], v[88:95], v[12:15]
	v_mfma_f32_16x16x128_f8f6f4 v[216:219], v[144:151], v[88:95], v[8:11]
	s_setprio 0
	s_setprio 1
	v_mfma_f32_16x16x128_f8f6f4 v[52:55], v[152:159], v[64:71], v[52:55]
	v_mfma_f32_16x16x128_f8f6f4 v[48:51], v[160:167], v[64:71], v[48:51]
	v_mfma_f32_16x16x128_f8f6f4 v[220:223], v[152:159], v[72:79], v[36:39]
	v_mfma_f32_16x16x128_f8f6f4 v[224:227], v[160:167], v[72:79], v[32:35]
	v_mfma_f32_16x16x128_f8f6f4 v[228:231], v[152:159], v[80:87], v[20:23]
	v_mfma_f32_16x16x128_f8f6f4 v[232:235], v[160:167], v[80:87], v[16:19]
	v_mfma_f32_16x16x128_f8f6f4 v[236:239], v[152:159], v[88:95], v[4:7]
	v_mfma_f32_16x16x128_f8f6f4 v[240:243], v[160:167], v[88:95], v[0:3]
	s_setprio 0
	s_barrier
	s_add_i32 s66, 0, 0x18000
	s_nop 2
	v_add_u32_e32 v4, s66, v244
	v_add_u32_e32 v8, s66, v245
	s_add_i32 s66, 0, 0x1c000
	ds_read_b128 v[0:3], v4
	ds_read_b128 v[16:19], v4 offset:2048
	ds_read_b128 v[4:7], v8
	ds_read_b128 v[20:23], v8 offset:2048
	v_add_u32_e32 v8, s66, v244
	v_add_u32_e32 v9, s66, v245
	ds_read_b128 v[136:139], v8
	ds_read_b128 v[144:147], v8 offset:2048
	ds_read_b128 v[140:143], v9
	ds_read_b128 v[148:151], v9 offset:2048
	s_mov_b32 m0, s33
	ds_read_b128 v[8:11], v250 offset:32768
	ds_read_b128 v[24:27], v250 offset:34816
	ds_read_b128 v[12:15], v251 offset:32768
	ds_read_b128 v[28:31], v251 offset:34816
	ds_read_b128 v[32:35], v250 offset:36864
	ds_read_b128 v[40:43], v250 offset:38912
	ds_read_b128 v[36:39], v251 offset:36864
	ds_read_b128 v[44:47], v251 offset:38912
	buffer_load_dwordx4 v248, s[8:11], s65 offen lds
	s_mov_b32 m0, s34
	s_nop 0
	buffer_load_dwordx4 v249, s[8:11], s65 offen lds
	s_waitcnt vmcnt(8)
	s_waitcnt lgkmcnt(0)
	s_barrier
	s_setprio 1
	s_waitcnt lgkmcnt(5)
	v_mfma_f32_16x16x128_f8f6f4 v[124:127], v[0:7], v[8:15], v[124:127]
	v_mfma_f32_16x16x128_f8f6f4 v[120:123], v[16:23], v[8:15], v[120:123]
	s_waitcnt lgkmcnt(4)
	v_mfma_f32_16x16x128_f8f6f4 v[108:111], v[0:7], v[24:31], v[108:111]
	v_mfma_f32_16x16x128_f8f6f4 v[104:107], v[16:23], v[24:31], v[104:107]
	s_waitcnt lgkmcnt(1)
	v_mfma_f32_16x16x128_f8f6f4 v[92:95], v[0:7], v[32:39], v[128:131]
	v_mfma_f32_16x16x128_f8f6f4 v[88:91], v[16:23], v[32:39], v[200:203]
	s_waitcnt lgkmcnt(0)
	v_mfma_f32_16x16x128_f8f6f4 v[76:79], v[0:7], v[40:47], v[204:207]
	v_mfma_f32_16x16x128_f8f6f4 v[72:75], v[16:23], v[40:47], v[208:211]
	s_setprio 0
	s_setprio 1
	v_mfma_f32_16x16x128_f8f6f4 v[116:119], v[136:143], v[8:15], v[116:119]
	v_mfma_f32_16x16x128_f8f6f4 v[112:115], v[144:151], v[8:15], v[112:115]
	v_mfma_f32_16x16x128_f8f6f4 v[100:103], v[136:143], v[24:31], v[100:103]
	v_mfma_f32_16x16x128_f8f6f4 v[96:99], v[144:151], v[24:31], v[96:99]
	v_mfma_f32_16x16x128_f8f6f4 v[84:87], v[136:143], v[32:39], v[168:171]
	v_mfma_f32_16x16x128_f8f6f4 v[80:83], v[144:151], v[32:39], v[172:175]
	v_mfma_f32_16x16x128_f8f6f4 v[68:71], v[136:143], v[40:47], v[176:179]
	v_mfma_f32_16x16x128_f8f6f4 v[64:67], v[144:151], v[40:47], v[180:183]
	s_setprio 0
	s_barrier
	s_mov_b32 m0, s36
	s_add_i32 s65, s63, 0x80
	ds_read_b128 v[32:35], v250 offset:49152
	ds_read_b128 v[152:155], v250 offset:51200
	ds_read_b128 v[36:39], v251 offset:49152
	ds_read_b128 v[156:159], v251 offset:51200
	ds_read_b128 v[160:163], v250 offset:53248
	ds_read_b128 v[168:171], v250 offset:55296
	ds_read_b128 v[164:167], v251 offset:53248
	ds_read_b128 v[172:175], v251 offset:55296
	buffer_load_dwordx4 v132, s[4:7], s65 offen lds
	s_mov_b32 m0, s37
	s_add_i32 s63, s63, 0x40080
	buffer_load_dwordx4 v133, s[4:7], s65 offen lds
	s_mov_b32 m0, s40
	s_nop 0
	buffer_load_dwordx4 v132, s[4:7], s63 offen lds
	s_mov_b32 m0, s41
	s_nop 0
	buffer_load_dwordx4 v133, s[4:7], s63 offen lds
	s_mov_b32 m0, s38
	s_nop 0
	buffer_load_dwordx4 v246, s[8:11], s64 offen lds
	s_mov_b32 m0, s39
	s_nop 0
	buffer_load_dwordx4 v247, s[8:11], s64 offen lds
	s_waitcnt vmcnt(8)
	s_waitcnt lgkmcnt(0)
	s_barrier
	s_setprio 1
	s_waitcnt lgkmcnt(5)
	v_mfma_f32_16x16x128_f8f6f4 v[60:63], v[0:7], v[32:39], v[60:63]
	v_mfma_f32_16x16x128_f8f6f4 v[56:59], v[16:23], v[32:39], v[56:59]
	s_waitcnt lgkmcnt(4)
	v_mfma_f32_16x16x128_f8f6f4 v[44:47], v[0:7], v[152:159], v[184:187]
	v_mfma_f32_16x16x128_f8f6f4 v[40:43], v[16:23], v[152:159], v[188:191]
	s_waitcnt lgkmcnt(1)
	v_mfma_f32_16x16x128_f8f6f4 v[28:31], v[0:7], v[160:167], v[192:195]
	v_mfma_f32_16x16x128_f8f6f4 v[24:27], v[16:23], v[160:167], v[196:199]
	s_waitcnt lgkmcnt(0)
	v_mfma_f32_16x16x128_f8f6f4 v[12:15], v[0:7], v[168:175], v[212:215]
	v_mfma_f32_16x16x128_f8f6f4 v[8:11], v[16:23], v[168:175], v[216:219]
	s_setprio 0
	s_setprio 1
	v_mfma_f32_16x16x128_f8f6f4 v[52:55], v[136:143], v[32:39], v[52:55]
	v_mfma_f32_16x16x128_f8f6f4 v[48:51], v[144:151], v[32:39], v[48:51]
	v_mfma_f32_16x16x128_f8f6f4 v[36:39], v[136:143], v[152:159], v[220:223]
	v_mfma_f32_16x16x128_f8f6f4 v[32:35], v[144:151], v[152:159], v[224:227]
	v_mfma_f32_16x16x128_f8f6f4 v[20:23], v[136:143], v[160:167], v[228:231]
	v_mfma_f32_16x16x128_f8f6f4 v[16:19], v[144:151], v[160:167], v[232:235]
	v_mfma_f32_16x16x128_f8f6f4 v[4:7], v[136:143], v[168:175], v[236:239]
	v_mfma_f32_16x16x128_f8f6f4 v[0:3], v[144:151], v[168:175], v[240:243]
	s_setprio 0
	s_barrier
	s_add_i32 s61, s61, 2
	s_addk_i32 s62, 0x100
	s_cmp_gt_u32 s61, 13
	s_cbranch_scc1 .LBB0_2177
	s_cmpk_lg_i32 s62, 0x780
	s_cbranch_scc1 .Lp5_fast

.Lp6_join:
	ds_read_b128 v[128:131], v132
	ds_read_b128 v[136:139], v132 offset:2048
	ds_read_b128 v[132:135], v140
	ds_read_b128 v[140:143], v140 offset:2048
	v_add_u32_e32 v155, s52, v246
	ds_read_b128 v[144:147], v148
	ds_read_b128 v[160:163], v148 offset:2048
	ds_read_b128 v[148:151], v155
	ds_read_b128 v[164:167], v155 offset:2048
	s_mov_b32 m0, s46
	ds_read_b128 v[168:171], v251
	ds_read_b128 v[176:179], v251 offset:2048
	ds_read_b128 v[172:175], v252
	ds_read_b128 v[180:183], v252 offset:2048
	ds_read_b128 v[184:187], v251 offset:4096
	ds_read_b128 v[192:195], v251 offset:6144
	ds_read_b128 v[188:191], v252 offset:4096
	ds_read_b128 v[196:199], v252 offset:6144
	s_add_i32 s6, s64, 0xffffff80
	s_add_i32 s7, s6, s59
	s_cmpk_eq_i32 s64, 0x880
	s_cselect_b32 s67, s37, s56
	s_cselect_b32 s6, 0, s6
	s_cselect_b32 s66, 0x80, s64
	s_cselect_b32 s65, s31, s7
	s_add_i32 s7, s56, s64
	s_add_i32 s66, s67, s66
	s_addk_i32 s7, 0xff00
	s_add_i32 s67, s67, s6
	buffer_load_dwordx4 v249, s[8:11], s7 offen lds
	s_mov_b32 m0, s49
	s_nop 0
	buffer_load_dwordx4 v250, s[8:11], s7 offen lds
	s_waitcnt vmcnt(8)
	s_waitcnt lgkmcnt(0)
	s_barrier
	s_setprio 1
	s_waitcnt lgkmcnt(5)
	v_mfma_f32_16x16x128_f8f6f4 v[124:127], v[128:135], v[168:175], v[124:127]
	v_mfma_f32_16x16x128_f8f6f4 v[120:123], v[136:143], v[168:175], v[120:123]
	s_waitcnt lgkmcnt(4)
	v_mfma_f32_16x16x128_f8f6f4 v[108:111], v[128:135], v[176:183], v[108:111]
	v_mfma_f32_16x16x128_f8f6f4 v[104:107], v[136:143], v[176:183], v[104:107]
	s_waitcnt lgkmcnt(1)
	v_mfma_f32_16x16x128_f8f6f4 v[152:155], v[128:135], v[184:191], v[92:95]
	v_mfma_f32_16x16x128_f8f6f4 v[200:203], v[136:143], v[184:191], v[88:91]
	s_waitcnt lgkmcnt(0)
	v_mfma_f32_16x16x128_f8f6f4 v[204:207], v[128:135], v[192:199], v[76:79]
	v_mfma_f32_16x16x128_f8f6f4 v[208:211], v[136:143], v[192:199], v[72:75]
	s_setprio 0
	s_setprio 1
	v_mfma_f32_16x16x128_f8f6f4 v[116:119], v[144:151], v[168:175], v[116:119]
	v_mfma_f32_16x16x128_f8f6f4 v[112:115], v[160:167], v[168:175], v[112:115]
	v_mfma_f32_16x16x128_f8f6f4 v[100:103], v[144:151], v[176:183], v[100:103]
	v_mfma_f32_16x16x128_f8f6f4 v[96:99], v[160:167], v[176:183], v[96:99]
	v_mfma_f32_16x16x128_f8f6f4 v[168:171], v[144:151], v[184:191], v[84:87]
	v_mfma_f32_16x16x128_f8f6f4 v[172:175], v[160:167], v[184:191], v[80:83]
	v_mfma_f32_16x16x128_f8f6f4 v[176:179], v[144:151], v[192:199], v[68:71]
	v_mfma_f32_16x16x128_f8f6f4 v[180:183], v[160:167], v[192:199], v[64:67]
	s_setprio 0
	s_barrier
	s_mov_b32 m0, s28
	s_mov_b32 s6, s10
	s_mov_b32 s7, s11
	s_nop 1
	ds_read_b128 v[64:67], v251 offset:16384
	ds_read_b128 v[72:75], v251 offset:18432
	ds_read_b128 v[68:71], v252 offset:16384
	ds_read_b128 v[76:79], v252 offset:18432
	ds_read_b128 v[80:83], v251 offset:20480
	ds_read_b128 v[88:91], v251 offset:22528
	ds_read_b128 v[84:87], v252 offset:20480
	ds_read_b128 v[92:95], v252 offset:22528
	buffer_load_dwordx4 v159, s[4:7], s65 offen lds
	s_mov_b32 m0, s29
	s_add_i32 s68, s65, 0x40000
	buffer_load_dwordx4 v244, s[4:7], s65 offen lds
	s_mov_b32 m0, s30
	s_nop 0
	buffer_load_dwordx4 v159, s[4:7], s68 offen lds
	s_mov_b32 m0, s33
	s_nop 0
	buffer_load_dwordx4 v244, s[4:7], s68 offen lds
	s_mov_b32 m0, s27
	s_nop 0
	buffer_load_dwordx4 v247, s[8:11], s67 offen lds
	s_mov_b32 m0, s34
	s_nop 0
	buffer_load_dwordx4 v248, s[8:11], s67 offen lds
	s_waitcnt vmcnt(8)
	s_waitcnt lgkmcnt(0)
	s_barrier
	s_setprio 1
	s_waitcnt lgkmcnt(5)
	v_mfma_f32_16x16x128_f8f6f4 v[60:63], v[128:135], v[64:71], v[60:63]
	v_mfma_f32_16x16x128_f8f6f4 v[56:59], v[136:143], v[64:71], v[56:59]
	s_waitcnt lgkmcnt(4)
	v_mfma_f32_16x16x128_f8f6f4 v[184:187], v[128:135], v[72:79], v[44:47]
	v_mfma_f32_16x16x128_f8f6f4 v[188:191], v[136:143], v[72:79], v[40:43]
	s_waitcnt lgkmcnt(1)
	v_mfma_f32_16x16x128_f8f6f4 v[192:195], v[128:135], v[80:87], v[28:31]
	v_mfma_f32_16x16x128_f8f6f4 v[196:199], v[136:143], v[80:87], v[24:27]
	s_waitcnt lgkmcnt(0)
	v_mfma_f32_16x16x128_f8f6f4 v[212:215], v[128:135], v[88:95], v[12:15]
	v_mfma_f32_16x16x128_f8f6f4 v[216:219], v[136:143], v[88:95], v[8:11]
	s_setprio 0
	s_setprio 1
	v_mfma_f32_16x16x128_f8f6f4 v[52:55], v[144:151], v[64:71], v[52:55]
	v_mfma_f32_16x16x128_f8f6f4 v[48:51], v[160:167], v[64:71], v[48:51]
	v_mfma_f32_16x16x128_f8f6f4 v[220:223], v[144:151], v[72:79], v[36:39]
	v_mfma_f32_16x16x128_f8f6f4 v[224:227], v[160:167], v[72:79], v[32:35]
	v_mfma_f32_16x16x128_f8f6f4 v[228:231], v[144:151], v[80:87], v[20:23]
	v_mfma_f32_16x16x128_f8f6f4 v[232:235], v[160:167], v[80:87], v[16:19]
	v_mfma_f32_16x16x128_f8f6f4 v[236:239], v[144:151], v[88:95], v[4:7]
	v_mfma_f32_16x16x128_f8f6f4 v[240:243], v[160:167], v[88:95], v[0:3]
	s_setprio 0
	s_barrier
	s_add_i32 s68, 0, 0x18000
	s_nop 2
	v_add_u32_e32 v4, s68, v245
	v_add_u32_e32 v8, s68, v246
	s_add_i32 s68, 0, 0x1c000
	ds_read_b128 v[0:3], v4
	ds_read_b128 v[16:19], v4 offset:2048
	ds_read_b128 v[4:7], v8
	ds_read_b128 v[20:23], v8 offset:2048
	v_add_u32_e32 v8, s68, v245
	v_add_u32_e32 v9, s68, v246
	ds_read_b128 v[128:131], v8
	ds_read_b128 v[136:139], v8 offset:2048
	ds_read_b128 v[132:135], v9
	ds_read_b128 v[140:143], v9 offset:2048
	s_mov_b32 m0, s35
	ds_read_b128 v[8:11], v251 offset:32768
	ds_read_b128 v[24:27], v251 offset:34816
	ds_read_b128 v[12:15], v252 offset:32768
	ds_read_b128 v[28:31], v252 offset:34816
	ds_read_b128 v[32:35], v251 offset:36864
	ds_read_b128 v[40:43], v251 offset:38912
	ds_read_b128 v[36:39], v252 offset:36864
	ds_read_b128 v[44:47], v252 offset:38912
	buffer_load_dwordx4 v249, s[8:11], s67 offen lds
	s_mov_b32 m0, s36
	s_nop 0
	buffer_load_dwordx4 v250, s[8:11], s67 offen lds
	s_waitcnt vmcnt(8)
	s_waitcnt lgkmcnt(0)
	s_barrier
	s_setprio 1
	s_waitcnt lgkmcnt(5)
	v_mfma_f32_16x16x128_f8f6f4 v[124:127], v[0:7], v[8:15], v[124:127]
	v_mfma_f32_16x16x128_f8f6f4 v[120:123], v[16:23], v[8:15], v[120:123]
	s_waitcnt lgkmcnt(4)
	v_mfma_f32_16x16x128_f8f6f4 v[108:111], v[0:7], v[24:31], v[108:111]
	v_mfma_f32_16x16x128_f8f6f4 v[104:107], v[16:23], v[24:31], v[104:107]
	s_waitcnt lgkmcnt(1)
	v_mfma_f32_16x16x128_f8f6f4 v[92:95], v[0:7], v[32:39], v[152:155]
	v_mfma_f32_16x16x128_f8f6f4 v[88:91], v[16:23], v[32:39], v[200:203]
	s_waitcnt lgkmcnt(0)
	v_mfma_f32_16x16x128_f8f6f4 v[76:79], v[0:7], v[40:47], v[204:207]
	v_mfma_f32_16x16x128_f8f6f4 v[72:75], v[16:23], v[40:47], v[208:211]
	s_setprio 0
	s_setprio 1
	v_mfma_f32_16x16x128_f8f6f4 v[116:119], v[128:135], v[8:15], v[116:119]
	v_mfma_f32_16x16x128_f8f6f4 v[112:115], v[136:143], v[8:15], v[112:115]
	v_mfma_f32_16x16x128_f8f6f4 v[100:103], v[128:135], v[24:31], v[100:103]
	v_mfma_f32_16x16x128_f8f6f4 v[96:99], v[136:143], v[24:31], v[96:99]
	v_mfma_f32_16x16x128_f8f6f4 v[84:87], v[128:135], v[32:39], v[168:171]
	v_mfma_f32_16x16x128_f8f6f4 v[80:83], v[136:143], v[32:39], v[172:175]
	v_mfma_f32_16x16x128_f8f6f4 v[68:71], v[128:135], v[40:47], v[176:179]
	v_mfma_f32_16x16x128_f8f6f4 v[64:67], v[136:143], v[40:47], v[180:183]
	s_setprio 0
	s_barrier
	s_mov_b32 m0, s38
	s_add_i32 s67, s65, 0x80
	ds_read_b128 v[32:35], v251 offset:49152
	ds_read_b128 v[144:147], v251 offset:51200
	ds_read_b128 v[36:39], v252 offset:49152
	ds_read_b128 v[148:151], v252 offset:51200
	ds_read_b128 v[160:163], v251 offset:53248
	ds_read_b128 v[168:171], v251 offset:55296
	ds_read_b128 v[164:167], v252 offset:53248
	ds_read_b128 v[172:175], v252 offset:55296
	buffer_load_dwordx4 v159, s[4:7], s67 offen lds
	s_mov_b32 m0, s39
	s_add_i32 s65, s65, 0x40080
	buffer_load_dwordx4 v244, s[4:7], s67 offen lds
	s_mov_b32 m0, s42
	s_nop 0
	buffer_load_dwordx4 v159, s[4:7], s65 offen lds
	s_mov_b32 m0, s43
	s_nop 0
	buffer_load_dwordx4 v244, s[4:7], s65 offen lds
	s_mov_b32 m0, s40
	s_nop 0
	buffer_load_dwordx4 v247, s[8:11], s66 offen lds
	s_mov_b32 m0, s41
	s_nop 0
	buffer_load_dwordx4 v248, s[8:11], s66 offen lds
	s_waitcnt vmcnt(8)
	s_waitcnt lgkmcnt(0)
	s_barrier
	s_setprio 1
	s_waitcnt lgkmcnt(5)
	v_mfma_f32_16x16x128_f8f6f4 v[60:63], v[0:7], v[32:39], v[60:63]
	v_mfma_f32_16x16x128_f8f6f4 v[56:59], v[16:23], v[32:39], v[56:59]
	s_waitcnt lgkmcnt(4)
	v_mfma_f32_16x16x128_f8f6f4 v[44:47], v[0:7], v[144:151], v[184:187]
	v_mfma_f32_16x16x128_f8f6f4 v[40:43], v[16:23], v[144:151], v[188:191]
	s_waitcnt lgkmcnt(1)
	v_mfma_f32_16x16x128_f8f6f4 v[28:31], v[0:7], v[160:167], v[192:195]
	v_mfma_f32_16x16x128_f8f6f4 v[24:27], v[16:23], v[160:167], v[196:199]
	s_waitcnt lgkmcnt(0)
	v_mfma_f32_16x16x128_f8f6f4 v[12:15], v[0:7], v[168:175], v[212:215]
	v_mfma_f32_16x16x128_f8f6f4 v[8:11], v[16:23], v[168:175], v[216:219]
	s_setprio 0
	s_setprio 1
	v_mfma_f32_16x16x128_f8f6f4 v[52:55], v[128:135], v[32:39], v[52:55]
	v_mfma_f32_16x16x128_f8f6f4 v[48:51], v[136:143], v[32:39], v[48:51]
	v_mfma_f32_16x16x128_f8f6f4 v[36:39], v[128:135], v[144:151], v[220:223]
	v_mfma_f32_16x16x128_f8f6f4 v[32:35], v[136:143], v[144:151], v[224:227]
	v_mfma_f32_16x16x128_f8f6f4 v[20:23], v[128:135], v[160:167], v[228:231]
	v_mfma_f32_16x16x128_f8f6f4 v[16:19], v[136:143], v[160:167], v[232:235]
	v_mfma_f32_16x16x128_f8f6f4 v[4:7], v[128:135], v[168:175], v[236:239]
	v_mfma_f32_16x16x128_f8f6f4 v[0:3], v[136:143], v[168:175], v[240:243]
	s_setprio 0
	s_barrier
	s_add_i32 s63, s63, 2
	s_addk_i32 s64, 0x100
	s_cmp_gt_u32 s63, 13
	s_cbranch_scc1 .LBB0_2201
	s_cmpk_lg_i32 s64, 0x780
	s_cbranch_scc1 .Lp6_fast

.Lp7_join:
	ds_read_b128 v[128:131], v132
	ds_read_b128 v[138:141], v132 offset:2048
	ds_read_b128 v[132:135], v142
	ds_read_b128 v[142:145], v142 offset:2048
	ds_read_b128 v[146:149], v150
	ds_read_b128 v[154:157], v150 offset:2048
	ds_read_b128 v[150:153], v158
	ds_read_b128 v[158:161], v158 offset:2048
	s_mov_b32 m0, s44
	ds_read_b128 v[162:165], v250
	ds_read_b128 v[170:173], v250 offset:2048
	ds_read_b128 v[166:169], v251
	ds_read_b128 v[174:177], v251 offset:2048
	ds_read_b128 v[178:181], v250 offset:4096
	ds_read_b128 v[186:189], v250 offset:6144
	ds_read_b128 v[182:185], v251 offset:4096
	ds_read_b128 v[190:193], v251 offset:6144
	s_add_i32 s6, s61, 0xffffff80
	s_add_i32 s7, s6, s56
	s_cmpk_eq_i32 s61, 0x880
	s_cselect_b32 s64, s35, s53
	s_cselect_b32 s6, 0, s6
	s_cselect_b32 s63, 0x80, s61
	s_cselect_b32 s62, s29, s7
	s_add_i32 s7, s53, s61
	s_add_i32 s63, s64, s63
	s_addk_i32 s7, 0xff00
	s_add_i32 s64, s64, s6
	buffer_load_dwordx4 v248, s[8:11], s7 offen lds
	s_mov_b32 m0, s47
	s_nop 0
	buffer_load_dwordx4 v249, s[8:11], s7 offen lds
	s_waitcnt vmcnt(8)
	s_waitcnt lgkmcnt(0)
	s_barrier
	s_setprio 1
	s_waitcnt lgkmcnt(0)
	v_mfma_f32_16x16x128_f8f6f4 v[124:127], v[128:135], v[162:169], v[124:127]
	v_mfma_f32_16x16x128_f8f6f4 v[120:123], v[138:145], v[162:169], v[120:123]
	v_mfma_f32_16x16x128_f8f6f4 v[116:119], v[128:135], v[170:177], v[116:119]
	v_mfma_f32_16x16x128_f8f6f4 v[112:115], v[138:145], v[170:177], v[112:115]
	v_mfma_f32_16x16x128_f8f6f4 v[194:197], v[128:135], v[178:185], v[92:95]
	v_mfma_f32_16x16x128_f8f6f4 v[198:201], v[138:145], v[178:185], v[88:91]
	v_mfma_f32_16x16x128_f8f6f4 v[202:205], v[128:135], v[186:193], v[84:87]
	v_mfma_f32_16x16x128_f8f6f4 v[206:209], v[138:145], v[186:193], v[80:83]
	s_setprio 0
	s_setprio 1
	v_mfma_f32_16x16x128_f8f6f4 v[108:111], v[146:153], v[162:169], v[108:111]
	v_mfma_f32_16x16x128_f8f6f4 v[104:107], v[154:161], v[162:169], v[104:107]
	v_mfma_f32_16x16x128_f8f6f4 v[100:103], v[146:153], v[170:177], v[100:103]
	v_mfma_f32_16x16x128_f8f6f4 v[96:99], v[154:161], v[170:177], v[96:99]
	v_mfma_f32_16x16x128_f8f6f4 v[162:165], v[146:153], v[178:185], v[76:79]
	v_mfma_f32_16x16x128_f8f6f4 v[166:169], v[154:161], v[178:185], v[72:75]
	v_mfma_f32_16x16x128_f8f6f4 v[170:173], v[146:153], v[186:193], v[68:71]
	v_mfma_f32_16x16x128_f8f6f4 v[174:177], v[154:161], v[186:193], v[64:67]
	s_setprio 0
	s_barrier
	s_mov_b32 m0, s26
	s_mov_b32 s6, s10
	s_mov_b32 s7, s11
	s_nop 1
	ds_read_b128 v[64:67], v250 offset:16384
	ds_read_b128 v[72:75], v250 offset:18432
	ds_read_b128 v[68:71], v251 offset:16384
	ds_read_b128 v[76:79], v251 offset:18432
	ds_read_b128 v[80:83], v250 offset:20480
	ds_read_b128 v[88:91], v250 offset:22528
	ds_read_b128 v[84:87], v251 offset:20480
	ds_read_b128 v[92:95], v251 offset:22528
	buffer_load_dwordx4 v242, s[4:7], s62 offen lds
	s_mov_b32 m0, s27
	s_add_i32 s65, s62, 0x40000
	buffer_load_dwordx4 v243, s[4:7], s62 offen lds
	s_mov_b32 m0, s28
	s_nop 0
	buffer_load_dwordx4 v242, s[4:7], s65 offen lds
	s_mov_b32 m0, s30
	s_nop 0
	buffer_load_dwordx4 v243, s[4:7], s65 offen lds
	s_mov_b32 m0, s25
	s_nop 0
	buffer_load_dwordx4 v246, s[8:11], s64 offen lds
	s_mov_b32 m0, s31
	s_nop 0
	buffer_load_dwordx4 v247, s[8:11], s64 offen lds
	s_waitcnt vmcnt(8)
	s_waitcnt lgkmcnt(0)
	s_barrier
	s_setprio 1
	s_waitcnt lgkmcnt(5)
	v_mfma_f32_16x16x128_f8f6f4 v[60:63], v[128:135], v[64:71], v[60:63]
	v_mfma_f32_16x16x128_f8f6f4 v[56:59], v[138:145], v[64:71], v[56:59]
	s_waitcnt lgkmcnt(4)
	v_mfma_f32_16x16x128_f8f6f4 v[52:55], v[128:135], v[72:79], v[52:55]
	v_mfma_f32_16x16x128_f8f6f4 v[48:51], v[138:145], v[72:79], v[48:51]
	s_waitcnt lgkmcnt(1)
	v_mfma_f32_16x16x128_f8f6f4 v[178:181], v[128:135], v[80:87], v[28:31]
	v_mfma_f32_16x16x128_f8f6f4 v[182:185], v[138:145], v[80:87], v[24:27]
	s_waitcnt lgkmcnt(0)
	v_mfma_f32_16x16x128_f8f6f4 v[186:189], v[128:135], v[88:95], v[20:23]
	v_mfma_f32_16x16x128_f8f6f4 v[190:193], v[138:145], v[88:95], v[16:19]
	s_setprio 0
	s_setprio 1
	v_mfma_f32_16x16x128_f8f6f4 v[210:213], v[146:153], v[64:71], v[44:47]
	v_mfma_f32_16x16x128_f8f6f4 v[214:217], v[154:161], v[64:71], v[40:43]
	v_mfma_f32_16x16x128_f8f6f4 v[218:221], v[146:153], v[72:79], v[36:39]
	v_mfma_f32_16x16x128_f8f6f4 v[222:225], v[154:161], v[72:79], v[32:35]
	v_mfma_f32_16x16x128_f8f6f4 v[226:229], v[146:153], v[80:87], v[12:15]
	v_mfma_f32_16x16x128_f8f6f4 v[230:233], v[154:161], v[80:87], v[8:11]
	v_mfma_f32_16x16x128_f8f6f4 v[234:237], v[146:153], v[88:95], v[4:7]
	v_mfma_f32_16x16x128_f8f6f4 v[238:241], v[154:161], v[88:95], v[0:3]
	s_setprio 0
	s_barrier
	s_add_i32 s65, 0, 0x18000
	s_nop 2
	v_add_u32_e32 v4, s65, v244
	v_add_u32_e32 v12, s65, v245
	s_add_i32 s65, 0, 0x1c000
	v_add_u32_e32 v16, s65, v244
	ds_read_b128 v[0:3], v4
	ds_read_b128 v[8:11], v4 offset:2048
	ds_read_b128 v[4:7], v12
	ds_read_b128 v[12:15], v12 offset:2048
	v_add_u32_e32 v17, s65, v245
	ds_read_b128 v[128:131], v16
	ds_read_b128 v[138:141], v16 offset:2048
	ds_read_b128 v[132:135], v17
	ds_read_b128 v[142:145], v17 offset:2048
	s_mov_b32 m0, s33
	ds_read_b128 v[16:19], v250 offset:32768
	ds_read_b128 v[24:27], v250 offset:34816
	ds_read_b128 v[20:23], v251 offset:32768
	ds_read_b128 v[28:31], v251 offset:34816
	ds_read_b128 v[32:35], v250 offset:36864
	ds_read_b128 v[40:43], v250 offset:38912
	ds_read_b128 v[36:39], v251 offset:36864
	ds_read_b128 v[44:47], v251 offset:38912
	buffer_load_dwordx4 v248, s[8:11], s64 offen lds
	s_mov_b32 m0, s34
	s_nop 0
	buffer_load_dwordx4 v249, s[8:11], s64 offen lds
	s_waitcnt vmcnt(8)
	s_waitcnt lgkmcnt(0)
	s_barrier
	s_setprio 1
	s_waitcnt lgkmcnt(5)
	v_mfma_f32_16x16x128_f8f6f4 v[124:127], v[0:7], v[16:23], v[124:127]
	v_mfma_f32_16x16x128_f8f6f4 v[120:123], v[8:15], v[16:23], v[120:123]
	s_waitcnt lgkmcnt(4)
	v_mfma_f32_16x16x128_f8f6f4 v[116:119], v[0:7], v[24:31], v[116:119]
	v_mfma_f32_16x16x128_f8f6f4 v[112:115], v[8:15], v[24:31], v[112:115]
	s_waitcnt lgkmcnt(1)
	v_mfma_f32_16x16x128_f8f6f4 v[92:95], v[0:7], v[32:39], v[194:197]
	v_mfma_f32_16x16x128_f8f6f4 v[88:91], v[8:15], v[32:39], v[198:201]
	s_waitcnt lgkmcnt(0)
	v_mfma_f32_16x16x128_f8f6f4 v[84:87], v[0:7], v[40:47], v[202:205]
	v_mfma_f32_16x16x128_f8f6f4 v[80:83], v[8:15], v[40:47], v[206:209]
	s_setprio 0
	s_setprio 1
	v_mfma_f32_16x16x128_f8f6f4 v[108:111], v[128:135], v[16:23], v[108:111]
	v_mfma_f32_16x16x128_f8f6f4 v[104:107], v[138:145], v[16:23], v[104:107]
	v_mfma_f32_16x16x128_f8f6f4 v[100:103], v[128:135], v[24:31], v[100:103]
	v_mfma_f32_16x16x128_f8f6f4 v[96:99], v[138:145], v[24:31], v[96:99]
	v_mfma_f32_16x16x128_f8f6f4 v[76:79], v[128:135], v[32:39], v[162:165]
	v_mfma_f32_16x16x128_f8f6f4 v[72:75], v[138:145], v[32:39], v[166:169]
	v_mfma_f32_16x16x128_f8f6f4 v[68:71], v[128:135], v[40:47], v[170:173]
	v_mfma_f32_16x16x128_f8f6f4 v[64:67], v[138:145], v[40:47], v[174:177]
	s_setprio 0
	s_barrier
	s_mov_b32 m0, s36
	s_add_i32 s64, s62, 0x80
	ds_read_b128 v[32:35], v250 offset:49152
	ds_read_b128 v[146:149], v250 offset:51200
	ds_read_b128 v[36:39], v251 offset:49152
	ds_read_b128 v[150:153], v251 offset:51200
	ds_read_b128 v[154:157], v250 offset:53248
	ds_read_b128 v[162:165], v250 offset:55296
	ds_read_b128 v[158:161], v251 offset:53248
	ds_read_b128 v[166:169], v251 offset:55296
	buffer_load_dwordx4 v242, s[4:7], s64 offen lds
	s_mov_b32 m0, s37
	s_add_i32 s62, s62, 0x40080
	buffer_load_dwordx4 v243, s[4:7], s64 offen lds
	s_mov_b32 m0, s40
	s_nop 0
	buffer_load_dwordx4 v242, s[4:7], s62 offen lds
	s_mov_b32 m0, s41
	s_nop 0
	buffer_load_dwordx4 v243, s[4:7], s62 offen lds
	s_mov_b32 m0, s38
	s_nop 0
	buffer_load_dwordx4 v246, s[8:11], s63 offen lds
	s_mov_b32 m0, s39
	s_nop 0
	buffer_load_dwordx4 v247, s[8:11], s63 offen lds
	s_waitcnt vmcnt(8)
	s_waitcnt lgkmcnt(0)
	s_barrier
	s_setprio 1
	s_waitcnt lgkmcnt(5)
	v_mfma_f32_16x16x128_f8f6f4 v[60:63], v[0:7], v[32:39], v[60:63]
	v_mfma_f32_16x16x128_f8f6f4 v[56:59], v[8:15], v[32:39], v[56:59]
	s_waitcnt lgkmcnt(4)
	v_mfma_f32_16x16x128_f8f6f4 v[52:55], v[0:7], v[146:153], v[52:55]
	v_mfma_f32_16x16x128_f8f6f4 v[48:51], v[8:15], v[146:153], v[48:51]
	s_waitcnt lgkmcnt(1)
	v_mfma_f32_16x16x128_f8f6f4 v[28:31], v[0:7], v[154:161], v[178:181]
	v_mfma_f32_16x16x128_f8f6f4 v[24:27], v[8:15], v[154:161], v[182:185]
	s_waitcnt lgkmcnt(0)
	v_mfma_f32_16x16x128_f8f6f4 v[20:23], v[0:7], v[162:169], v[186:189]
	v_mfma_f32_16x16x128_f8f6f4 v[16:19], v[8:15], v[162:169], v[190:193]
	s_setprio 0
	s_setprio 1
	v_mfma_f32_16x16x128_f8f6f4 v[44:47], v[128:135], v[32:39], v[210:213]
	v_mfma_f32_16x16x128_f8f6f4 v[40:43], v[138:145], v[32:39], v[214:217]
	v_mfma_f32_16x16x128_f8f6f4 v[36:39], v[128:135], v[146:153], v[218:221]
	v_mfma_f32_16x16x128_f8f6f4 v[32:35], v[138:145], v[146:153], v[222:225]
	v_mfma_f32_16x16x128_f8f6f4 v[12:15], v[128:135], v[154:161], v[226:229]
	v_mfma_f32_16x16x128_f8f6f4 v[8:11], v[138:145], v[154:161], v[230:233]
	v_mfma_f32_16x16x128_f8f6f4 v[4:7], v[128:135], v[162:169], v[234:237]
	v_mfma_f32_16x16x128_f8f6f4 v[0:3], v[138:145], v[162:169], v[238:241]
	s_setprio 0
	s_barrier
	s_add_i32 s60, s60, 2
	s_addk_i32 s61, 0x100
	s_cmp_gt_u32 s60, 13
	s_cbranch_scc1 .LBB0_2279
	s_cmpk_lg_i32 s61, 0x780
	s_cbranch_scc1 .Lp7_fast

.Lp11_join:
	ds_read_b128 v[128:131], v132
	ds_read_b128 v[136:139], v132 offset:2048
	ds_read_b128 v[132:135], v140
	ds_read_b128 v[140:143], v140 offset:2048
	ds_read_b128 v[154:157], v158
	ds_read_b128 v[162:165], v158 offset:2048
	ds_read_b128 v[158:161], v166
	ds_read_b128 v[166:169], v166 offset:2048
	s_mov_b32 m0, s60
	ds_read_b128 v[170:173], v148
	ds_read_b128 v[178:181], v148 offset:2048
	ds_read_b128 v[174:177], v146
	ds_read_b128 v[182:185], v146 offset:2048
	ds_read_b128 v[186:189], v148 offset:4096
	ds_read_b128 v[194:197], v148 offset:6144
	ds_read_b128 v[190:193], v146 offset:4096
	ds_read_b128 v[198:201], v146 offset:6144
	s_add_i32 s6, s80, 0xffffff80
	s_add_i32 s7, s6, s75
	s_cmpk_eq_i32 s80, 0x880
	s_cselect_b32 s81, s71, s35
	s_cselect_b32 s11, 0x80, s80
	s_cselect_b32 s10, 0, s6
	s_cselect_b32 s6, s51, s7
	s_add_i32 s7, s81, s11
	s_add_i32 s11, s35, s80
	s_addk_i32 s11, 0xff00
	s_add_i32 s81, s81, s10
	buffer_load_dwordx4 v252, s[88:91], s11 offen lds
	s_mov_b32 m0, s63
	s_nop 0
	buffer_load_dwordx4 v253, s[88:91], s11 offen lds
	s_waitcnt vmcnt(8)
	s_waitcnt lgkmcnt(0)
	s_barrier
	s_setprio 1
	s_waitcnt lgkmcnt(0)
	v_mfma_f32_16x16x128_f8f6f4 v[124:127], v[128:135], v[170:177], v[124:127]
	v_mfma_f32_16x16x128_f8f6f4 v[120:123], v[136:143], v[170:177], v[120:123]
	v_mfma_f32_16x16x128_f8f6f4 v[116:119], v[128:135], v[178:185], v[116:119]
	v_mfma_f32_16x16x128_f8f6f4 v[112:115], v[136:143], v[178:185], v[112:115]
	v_mfma_f32_16x16x128_f8f6f4 v[96:99], v[128:135], v[186:193], v[96:99]
	v_mfma_f32_16x16x128_f8f6f4 v[202:205], v[136:143], v[186:193], v[88:91]
	v_mfma_f32_16x16x128_f8f6f4 v[206:209], v[128:135], v[194:201], v[80:83]
	v_mfma_f32_16x16x128_f8f6f4 v[210:213], v[136:143], v[194:201], v[72:75]
	s_setprio 0
	s_setprio 1
	v_mfma_f32_16x16x128_f8f6f4 v[108:111], v[154:161], v[170:177], v[108:111]
	v_mfma_f32_16x16x128_f8f6f4 v[104:107], v[162:169], v[170:177], v[104:107]
	v_mfma_f32_16x16x128_f8f6f4 v[100:103], v[154:161], v[178:185], v[100:103]
	v_mfma_f32_16x16x128_f8f6f4 v[170:173], v[162:169], v[178:185], v[92:95]
	v_mfma_f32_16x16x128_f8f6f4 v[174:177], v[154:161], v[186:193], v[84:87]
	v_mfma_f32_16x16x128_f8f6f4 v[178:181], v[162:169], v[186:193], v[76:79]
	v_mfma_f32_16x16x128_f8f6f4 v[182:185], v[154:161], v[194:201], v[68:71]
	v_mfma_f32_16x16x128_f8f6f4 v[186:189], v[162:169], v[194:201], v[64:67]
	s_setprio 0
	s_barrier
	s_mov_b32 m0, s43
	s_mov_b32 s10, s90
	s_mov_b32 s11, s91
	s_nop 1
	ds_read_b128 v[64:67], v148 offset:16384
	ds_read_b128 v[72:75], v148 offset:18432
	ds_read_b128 v[68:71], v146 offset:16384
	ds_read_b128 v[76:79], v146 offset:18432
	ds_read_b128 v[80:83], v148 offset:20480
	ds_read_b128 v[88:91], v148 offset:22528
	ds_read_b128 v[84:87], v146 offset:20480
	ds_read_b128 v[92:95], v146 offset:22528
	buffer_load_dwordx4 v144, s[8:11], s6 offen lds
	s_mov_b32 m0, s44
	s_add_i32 s82, s6, 0x40000
	buffer_load_dwordx4 v145, s[8:11], s6 offen lds
	s_mov_b32 m0, s45
	s_nop 0
	buffer_load_dwordx4 v144, s[8:11], s82 offen lds
	s_mov_b32 m0, s46
	s_nop 0
	buffer_load_dwordx4 v145, s[8:11], s82 offen lds
	s_mov_b32 m0, s42
	s_nop 0
	buffer_load_dwordx4 v250, s[88:91], s81 offen lds
	s_mov_b32 m0, s47
	s_nop 0
	buffer_load_dwordx4 v251, s[88:91], s81 offen lds
	s_waitcnt vmcnt(8)
	s_waitcnt lgkmcnt(0)
	s_barrier
	s_setprio 1
	s_waitcnt lgkmcnt(5)
	v_mfma_f32_16x16x128_f8f6f4 v[60:63], v[128:135], v[64:71], v[60:63]
	v_mfma_f32_16x16x128_f8f6f4 v[56:59], v[136:143], v[64:71], v[56:59]
	s_waitcnt lgkmcnt(4)
	v_mfma_f32_16x16x128_f8f6f4 v[48:51], v[128:135], v[72:79], v[48:51]
	v_mfma_f32_16x16x128_f8f6f4 v[190:193], v[136:143], v[72:79], v[40:43]
	s_waitcnt lgkmcnt(1)
	v_mfma_f32_16x16x128_f8f6f4 v[194:197], v[128:135], v[80:87], v[32:35]
	v_mfma_f32_16x16x128_f8f6f4 v[198:201], v[136:143], v[80:87], v[24:27]
	s_waitcnt lgkmcnt(0)
	v_mfma_f32_16x16x128_f8f6f4 v[214:217], v[128:135], v[88:95], v[16:19]
	v_mfma_f32_16x16x128_f8f6f4 v[218:221], v[136:143], v[88:95], v[8:11]
	s_setprio 0
	s_setprio 1
	v_mfma_f32_16x16x128_f8f6f4 v[52:55], v[154:161], v[64:71], v[52:55]
	v_mfma_f32_16x16x128_f8f6f4 v[222:225], v[162:169], v[64:71], v[44:47]
	v_mfma_f32_16x16x128_f8f6f4 v[226:229], v[154:161], v[72:79], v[36:39]
	v_mfma_f32_16x16x128_f8f6f4 v[230:233], v[162:169], v[72:79], v[28:31]
	v_mfma_f32_16x16x128_f8f6f4 v[234:237], v[154:161], v[80:87], v[20:23]
	v_mfma_f32_16x16x128_f8f6f4 v[238:241], v[162:169], v[80:87], v[12:15]
	v_mfma_f32_16x16x128_f8f6f4 v[242:245], v[154:161], v[88:95], v[4:7]
	v_mfma_f32_16x16x128_f8f6f4 v[246:249], v[162:169], v[88:95], v[0:3]
	s_setprio 0
	s_barrier
	s_add_i32 s82, 0, 0x18000
	s_nop 2
	v_add_u32_e32 v4, s82, v150
	v_add_u32_e32 v12, s82, v152
	s_add_i32 s82, 0, 0x1c000
	v_add_u32_e32 v16, s82, v150
	ds_read_b128 v[0:3], v4
	ds_read_b128 v[8:11], v4 offset:2048
	ds_read_b128 v[4:7], v12
	ds_read_b128 v[12:15], v12 offset:2048
	v_add_u32_e32 v17, s82, v152
	ds_read_b128 v[128:131], v16
	ds_read_b128 v[136:139], v16 offset:2048
	ds_read_b128 v[132:135], v17
	ds_read_b128 v[140:143], v17 offset:2048
	s_mov_b32 m0, s48
	ds_read_b128 v[16:19], v148 offset:32768
	ds_read_b128 v[24:27], v148 offset:34816
	ds_read_b128 v[20:23], v146 offset:32768
	ds_read_b128 v[28:31], v146 offset:34816
	ds_read_b128 v[32:35], v148 offset:36864
	ds_read_b128 v[40:43], v148 offset:38912
	ds_read_b128 v[36:39], v146 offset:36864
	ds_read_b128 v[44:47], v146 offset:38912
	buffer_load_dwordx4 v252, s[88:91], s81 offen lds
	s_mov_b32 m0, s49
	s_nop 0
	buffer_load_dwordx4 v253, s[88:91], s81 offen lds
	s_waitcnt vmcnt(8)
	s_waitcnt lgkmcnt(0)
	s_barrier
	s_setprio 1
	s_waitcnt lgkmcnt(5)
	v_mfma_f32_16x16x128_f8f6f4 v[124:127], v[0:7], v[16:23], v[124:127]
	v_mfma_f32_16x16x128_f8f6f4 v[120:123], v[8:15], v[16:23], v[120:123]
	s_waitcnt lgkmcnt(4)
	v_mfma_f32_16x16x128_f8f6f4 v[116:119], v[0:7], v[24:31], v[116:119]
	v_mfma_f32_16x16x128_f8f6f4 v[112:115], v[8:15], v[24:31], v[112:115]
	s_waitcnt lgkmcnt(1)
	v_mfma_f32_16x16x128_f8f6f4 v[96:99], v[0:7], v[32:39], v[96:99]
	v_mfma_f32_16x16x128_f8f6f4 v[88:91], v[8:15], v[32:39], v[202:205]
	s_waitcnt lgkmcnt(0)
	v_mfma_f32_16x16x128_f8f6f4 v[80:83], v[0:7], v[40:47], v[206:209]
	v_mfma_f32_16x16x128_f8f6f4 v[72:75], v[8:15], v[40:47], v[210:213]
	s_setprio 0
	s_setprio 1
	v_mfma_f32_16x16x128_f8f6f4 v[108:111], v[128:135], v[16:23], v[108:111]
	v_mfma_f32_16x16x128_f8f6f4 v[104:107], v[136:143], v[16:23], v[104:107]
	v_mfma_f32_16x16x128_f8f6f4 v[100:103], v[128:135], v[24:31], v[100:103]
	v_mfma_f32_16x16x128_f8f6f4 v[92:95], v[136:143], v[24:31], v[170:173]
	v_mfma_f32_16x16x128_f8f6f4 v[84:87], v[128:135], v[32:39], v[174:177]
	v_mfma_f32_16x16x128_f8f6f4 v[76:79], v[136:143], v[32:39], v[178:181]
	v_mfma_f32_16x16x128_f8f6f4 v[68:71], v[128:135], v[40:47], v[182:185]
	v_mfma_f32_16x16x128_f8f6f4 v[64:67], v[136:143], v[40:47], v[186:189]
	s_setprio 0
	s_barrier
	s_mov_b32 m0, s52
	s_add_i32 s81, s6, 0x80
	ds_read_b128 v[154:157], v148 offset:49152
	ds_read_b128 v[162:165], v148 offset:51200
	ds_read_b128 v[158:161], v146 offset:49152
	ds_read_b128 v[166:169], v146 offset:51200
	ds_read_b128 v[170:173], v148 offset:53248
	ds_read_b128 v[178:181], v148 offset:55296
	ds_read_b128 v[174:177], v146 offset:53248
	ds_read_b128 v[182:185], v146 offset:55296
	buffer_load_dwordx4 v144, s[8:11], s81 offen lds
	s_mov_b32 m0, s53
	s_add_i32 s6, s6, 0x40080
	buffer_load_dwordx4 v145, s[8:11], s81 offen lds
	s_mov_b32 m0, s56
	s_nop 0
	buffer_load_dwordx4 v144, s[8:11], s6 offen lds
	s_mov_b32 m0, s57
	s_nop 0
	buffer_load_dwordx4 v145, s[8:11], s6 offen lds
	s_mov_b32 m0, s54
	s_nop 0
	buffer_load_dwordx4 v250, s[88:91], s7 offen lds
	s_mov_b32 m0, s55
	s_nop 0
	buffer_load_dwordx4 v251, s[88:91], s7 offen lds
	s_waitcnt vmcnt(8)
	s_waitcnt lgkmcnt(0)
	s_barrier
	s_setprio 1
	s_waitcnt lgkmcnt(5)
	v_mfma_f32_16x16x128_f8f6f4 v[60:63], v[0:7], v[154:161], v[60:63]
	v_mfma_f32_16x16x128_f8f6f4 v[56:59], v[8:15], v[154:161], v[56:59]
	s_waitcnt lgkmcnt(4)
	v_mfma_f32_16x16x128_f8f6f4 v[48:51], v[0:7], v[162:169], v[48:51]
	v_mfma_f32_16x16x128_f8f6f4 v[40:43], v[8:15], v[162:169], v[190:193]
	s_waitcnt lgkmcnt(1)
	v_mfma_f32_16x16x128_f8f6f4 v[32:35], v[0:7], v[170:177], v[194:197]
	v_mfma_f32_16x16x128_f8f6f4 v[24:27], v[8:15], v[170:177], v[198:201]
	s_waitcnt lgkmcnt(0)
	v_mfma_f32_16x16x128_f8f6f4 v[16:19], v[0:7], v[178:185], v[214:217]
	v_mfma_f32_16x16x128_f8f6f4 v[8:11], v[8:15], v[178:185], v[218:221]
	s_setprio 0
	s_setprio 1
	v_mfma_f32_16x16x128_f8f6f4 v[52:55], v[128:135], v[154:161], v[52:55]
	v_mfma_f32_16x16x128_f8f6f4 v[44:47], v[136:143], v[154:161], v[222:225]
	v_mfma_f32_16x16x128_f8f6f4 v[36:39], v[128:135], v[162:169], v[226:229]
	v_mfma_f32_16x16x128_f8f6f4 v[28:31], v[136:143], v[162:169], v[230:233]
	v_mfma_f32_16x16x128_f8f6f4 v[20:23], v[128:135], v[170:177], v[234:237]
	v_mfma_f32_16x16x128_f8f6f4 v[12:15], v[136:143], v[170:177], v[238:241]
	v_mfma_f32_16x16x128_f8f6f4 v[4:7], v[128:135], v[178:185], v[242:245]
	v_mfma_f32_16x16x128_f8f6f4 v[0:3], v[136:143], v[178:185], v[246:249]
	s_setprio 0
	s_barrier
	s_add_i32 s79, s79, 2
	s_addk_i32 s80, 0x100
	s_cmp_gt_u32 s79, 13
	s_cbranch_scc1 .LBB0_2574
	s_cmpk_lg_i32 s80, 0x780
	s_cbranch_scc1 .Lp11_fast
